# speedup vs baseline: 1.0696x; 1.0401x over previous
_Z11k_chunksortPKiS0_PjS1_PKfS3_S3_S3_S3_PDF16_S4_PfS5_S4_Ph:
	s_cmpk_lt_i32 s2, 0x7d
	s_mov_b64 s[4:5], -1
	s_cbranch_scc0 .LBB0_13
	s_load_dwordx4 s[4:7], s[0:1], 0x0
	s_mul_i32 s3, s2, 0x1400
	v_or_b32_e32 v2, s3, v0
	v_ashrrev_i32_e32 v3, 31, v2
	v_lshlrev_b64 v[4:5], 2, v[2:3]
	s_waitcnt lgkmcnt(0)
	v_lshl_add_u64 v[6:7], s[4:5], 0, v[4:5]
	v_lshl_add_u64 v[4:5], s[6:7], 0, v[4:5]
	global_load_dword v12, v[4:5], off nt
	v_add_u32_e32 v4, 0x400, v2
	v_ashrrev_i32_e32 v5, 31, v4
	global_load_dword v13, v[6:7], off nt
	v_lshlrev_b64 v[6:7], 2, v[4:5]
	v_lshl_add_u64 v[8:9], s[4:5], 0, v[6:7]
	v_lshl_add_u64 v[6:7], s[6:7], 0, v[6:7]
	global_load_dword v14, v[6:7], off nt
	v_add_u32_e32 v6, 0x800, v2
	v_ashrrev_i32_e32 v7, 31, v6
	global_load_dword v15, v[8:9], off nt
	v_lshlrev_b64 v[8:9], 2, v[6:7]
	v_lshl_add_u64 v[10:11], s[4:5], 0, v[8:9]
	v_lshl_add_u64 v[8:9], s[6:7], 0, v[8:9]
	global_load_dword v16, v[8:9], off nt
	v_add_u32_e32 v8, 0xc00, v2
	v_ashrrev_i32_e32 v9, 31, v8
	global_load_dword v17, v[10:11], off nt
	v_lshlrev_b64 v[10:11], 2, v[8:9]
	v_lshl_add_u64 v[18:19], s[4:5], 0, v[10:11]
	v_lshl_add_u64 v[10:11], s[6:7], 0, v[10:11]
	global_load_dword v19, v[18:19], off nt
	s_movk_i32 s3, 0x100
	global_load_dword v18, v[10:11], off nt
	v_add_u32_e32 v10, 0x1000, v2
	v_ashrrev_i32_e32 v11, 31, v10
	v_lshlrev_b64 v[22:23], 2, v[10:11]
	v_lshl_add_u64 v[20:21], s[4:5], 0, v[22:23]
	v_lshl_add_u64 v[22:23], s[6:7], 0, v[22:23]
	global_load_dword v21, v[20:21], off nt
	v_cmp_gt_u32_e32 vcc, s3, v0
	global_load_dword v20, v[22:23], off nt
	v_lshlrev_b32_e32 v1, 2, v0
	s_and_saveexec_b64 s[4:5], vcc
	v_mov_b32_e32 v22, 0
	ds_write_b32 v1, v22 offset:20480
	s_or_b64 exec, exec, s[4:5]
	s_mov_b32 s3, 0x14e5e0b
	s_waitcnt vmcnt(9)
	v_mul_hi_u32 v26, v12, s3
	v_lshlrev_b32_e32 v27, 2, v26
	v_mov_b32_e32 v29, 1
	s_waitcnt vmcnt(7)
	v_mul_hi_u32 v25, v14, s3
	s_waitcnt lgkmcnt(0)
	s_barrier
	ds_add_u32 v27, v29 offset:20480
	v_lshlrev_b32_e32 v28, 2, v25
	s_waitcnt vmcnt(5)
	v_mul_hi_u32 v24, v16, s3
	ds_add_u32 v28, v29 offset:20480
	v_lshlrev_b32_e32 v30, 2, v24
	s_waitcnt vmcnt(2)
	v_mul_hi_u32 v23, v18, s3
	ds_add_u32 v30, v29 offset:20480
	v_lshlrev_b32_e32 v31, 2, v23
	s_waitcnt vmcnt(0)
	v_mul_hi_u32 v22, v20, s3
	ds_add_u32 v31, v29 offset:20480
	v_lshlrev_b32_e32 v32, 2, v22
	ds_add_u32 v32, v29 offset:20480
	v_mov_b32_e32 v29, 0
	s_waitcnt lgkmcnt(0)
	s_barrier
	s_and_saveexec_b64 s[4:5], vcc
	ds_read_b32 v29, v1 offset:20480
	s_or_b64 exec, exec, s[4:5]
	v_mbcnt_lo_u32_b32 v33, -1, 0
	v_mbcnt_hi_u32_b32 v33, -1, v33
	v_and_b32_e32 v34, 64, v33
	v_add_u32_e32 v35, -1, v33
	v_cmp_lt_i32_e64 s[4:5], v35, v34
	v_and_b32_e32 v36, 63, v0
	v_add_u32_e32 v37, -2, v33
	v_cndmask_b32_e64 v35, v35, v33, s[4:5]
	v_lshlrev_b32_e32 v35, 2, v35
	s_waitcnt lgkmcnt(0)
	ds_bpermute_b32 v35, v35, v29
	v_cmp_ne_u32_e64 s[4:5], 0, v36
	s_waitcnt lgkmcnt(0)
	s_nop 0
	v_cndmask_b32_e64 v35, 0, v35, s[4:5]
	v_cmp_lt_i32_e64 s[4:5], v37, v34
	v_add_u32_e32 v35, v35, v29
	s_nop 0
	v_cndmask_b32_e64 v37, v37, v33, s[4:5]
	v_lshlrev_b32_e32 v37, 2, v37
	ds_bpermute_b32 v37, v37, v35
	v_cmp_lt_u32_e64 s[4:5], 1, v36
	s_waitcnt lgkmcnt(0)
	s_nop 0
	v_cndmask_b32_e64 v37, 0, v37, s[4:5]
	v_add_u32_e32 v35, v37, v35
	v_add_u32_e32 v37, -4, v33
	v_cmp_lt_i32_e64 s[4:5], v37, v34
	s_nop 1
	v_cndmask_b32_e64 v37, v37, v33, s[4:5]
	v_lshlrev_b32_e32 v37, 2, v37
	ds_bpermute_b32 v37, v37, v35
	v_cmp_lt_u32_e64 s[4:5], 3, v36
	s_waitcnt lgkmcnt(0)
	s_nop 0
	v_cndmask_b32_e64 v37, 0, v37, s[4:5]
	v_add_u32_e32 v35, v37, v35
	v_add_u32_e32 v37, -8, v33
	v_cmp_lt_i32_e64 s[4:5], v37, v34
	s_nop 1
	v_cndmask_b32_e64 v37, v37, v33, s[4:5]
	v_lshlrev_b32_e32 v37, 2, v37
	ds_bpermute_b32 v37, v37, v35
	v_cmp_lt_u32_e64 s[4:5], 7, v36
	s_waitcnt lgkmcnt(0)
	s_nop 0
	v_cndmask_b32_e64 v37, 0, v37, s[4:5]
	v_add_u32_e32 v35, v37, v35
	v_add_u32_e32 v37, -16, v33
	v_cmp_lt_i32_e64 s[4:5], v37, v34
	s_nop 1
	v_cndmask_b32_e64 v37, v37, v33, s[4:5]
	v_lshlrev_b32_e32 v37, 2, v37
	ds_bpermute_b32 v37, v37, v35
	v_cmp_lt_u32_e64 s[4:5], 15, v36
	s_waitcnt lgkmcnt(0)
	s_nop 0
	v_cndmask_b32_e64 v37, 0, v37, s[4:5]
	v_add_u32_e32 v35, v37, v35
	v_subrev_u32_e32 v37, 32, v33
	v_cmp_lt_i32_e64 s[4:5], v37, v34
	v_and_b32_e32 v34, 0x33f, v0
	s_nop 0
	v_cndmask_b32_e64 v33, v37, v33, s[4:5]
	v_lshlrev_b32_e32 v33, 2, v33
	ds_bpermute_b32 v33, v33, v35
	v_cmp_lt_u32_e64 s[4:5], 31, v36
	s_waitcnt lgkmcnt(0)
	s_nop 0
	v_cndmask_b32_e64 v33, 0, v33, s[4:5]
	v_add_u32_e32 v33, v33, v35
	v_cmp_eq_u32_e64 s[4:5], 63, v34
	s_and_saveexec_b64 s[6:7], s[4:5]
	v_lshrrev_b32_e32 v34, 4, v0
	v_and_b32_e32 v34, 60, v34
	ds_write_b32 v34, v33 offset:21504
	s_or_b64 exec, exec, s[6:7]
	s_load_dwordx2 s[6:7], s[0:1], 0x18
	s_waitcnt lgkmcnt(0)
	s_barrier
	s_and_saveexec_b64 s[8:9], vcc
	s_cbranch_execz .LBB0_9
	v_mov_b32_e32 v34, 0
	ds_read_b96 v[34:36], v34 offset:21504
	s_movk_i32 s3, 0x7f
	v_cmp_lt_u32_e64 s[4:5], 63, v0
	s_waitcnt lgkmcnt(0)
	s_nop 0
	v_cndmask_b32_e64 v34, 0, v34, s[4:5]
	v_cmp_lt_u32_e64 s[4:5], s3, v0
	s_movk_i32 s3, 0xbf
	v_add_u32_e32 v33, v34, v33
	v_cndmask_b32_e64 v35, 0, v35, s[4:5]
	v_cmp_lt_u32_e64 s[4:5], s3, v0
	s_nop 1
	v_cndmask_b32_e64 v36, 0, v36, s[4:5]
	v_add3_u32 v33, v33, v35, v36

_Z5k_csrPKjS0_PKfPjPfPDF16_P15HIP_vector_typeIjLj4EE:
	s_load_dwordx2 s[4:5], s[0:1], 0x0
	s_load_dwordx2 s[6:7], s[0:1], 0x10
	s_mul_i32 s3, s2, 0xc4
	v_lshrrev_b32_e32 v25, 4, v0
	v_add_u32_e32 v28, s3, v25
	v_and_b32_e32 v1, 15, v0
	v_min_i32_e32 v4, 0xc34f, v28
	v_add_u32_e32 v26, 64, v28
	v_lshlrev_b32_e32 v18, 4, v1
	v_mov_b32_e32 v19, 0
	v_ashrrev_i32_e32 v5, 31, v4
	v_min_i32_e32 v6, 0xc34f, v26
	s_waitcnt lgkmcnt(0)
	v_lshl_add_u64 v[2:3], s[6:7], 0, v[18:19]
	v_lshlrev_b64 v[4:5], 8, v[4:5]
	v_ashrrev_i32_e32 v7, 31, v6
	v_lshl_add_u64 v[4:5], v[2:3], 0, v[4:5]
	v_lshlrev_b64 v[6:7], 8, v[6:7]
	v_add_u32_e32 v24, 0x80, v28
	v_lshl_add_u64 v[6:7], v[2:3], 0, v[6:7]
	global_load_dwordx4 v[14:17], v[4:5], off nt
	global_load_dwordx4 v[10:13], v[6:7], off nt
	v_min_i32_e32 v4, 0xc34f, v24
	v_or_b32_e32 v32, 0xc00, v0
	v_ashrrev_i32_e32 v5, 31, v4
	v_lshrrev_b32_e32 v23, 4, v32
	v_lshlrev_b64 v[4:5], 8, v[4:5]
	v_add_u32_e32 v22, s3, v23
	v_lshl_add_u64 v[20:21], v[2:3], 0, v[4:5]
	v_min_i32_e32 v4, 0xc34f, v22
	v_ashrrev_i32_e32 v5, 31, v4
	v_lshlrev_b64 v[4:5], 8, v[4:5]
	v_lshrrev_b32_e32 v1, 3, v0
	v_lshl_add_u64 v[30:31], v[2:3], 0, v[4:5]
	global_load_dwordx4 v[6:9], v[20:21], off nt
	global_load_dwordx4 v[2:5], v[30:31], off nt
	v_min_u32_e32 v20, 0x7c, v1
	s_mul_i32 s6, s2, 0x7d
	v_add_u32_e32 v30, s6, v20
	v_ashrrev_i32_e32 v31, 31, v30
	v_lshl_add_u64 v[30:31], v[30:31], 2, s[4:5]
	global_load_dword v21, v[30:31], off
	global_load_dword v27, v[30:31], off offset:500
	v_cmp_gt_u32_e32 vcc, 2, v0
	v_lshlrev_b32_e32 v1, 2, v0
	s_and_saveexec_b64 s[4:5], vcc
	v_lshlrev_b32_e32 v18, 2, v0
	ds_write_b32 v18, v19 offset:22528
	s_or_b64 exec, exec, s[4:5]
	s_movk_i32 s4, 0x100
	v_cmp_gt_u32_e64 s[8:9], s4, v0
	s_and_saveexec_b64 s[4:5], s[8:9]
	s_cbranch_execz .LBB1_4
	s_mov_b32 s6, 0x539782a
	v_mul_hi_u32 v29, v0, s6
	s_movk_i32 s6, 0xffcf
	v_lshlrev_b32_e32 v18, 2, v0
	v_mov_b32_e32 v19, 0
	v_mad_i32_i24 v29, v29, s6, v0
	ds_write2st64_b32 v18, v19, v29 offset0:64 offset1:72
